# v23 + the workgroups idle in GEMM2's partial last round also pull the first 64 MiB of Y (oldest GEMM2 rows) into the Infinity Cache after the x1 copy
# baseline (speedup 1.0000x reference)
.LBB0_841:
	s_xor_b32 s4, s6, s4
	s_mul_i32 s6, s5, s1
	s_sub_i32 s6, s7, s6
	s_add_i32 s7, s5, 1
	s_sub_i32 s13, s6, s1
	s_cmp_ge_u32 s6, s1
	s_cselect_b32 s5, s7, s5
	s_cselect_b32 s6, s13, s6
	s_add_i32 s7, s5, 1
	s_cmp_ge_u32 s6, s1
	s_cselect_b32 s1, s7, s5
	s_xor_b32 s1, s1, s4
	s_not_b32 s4, s4
	s_add_i32 s1, s4, s1
	s_mul_i32 s1, s1, s56
	s_add_i32 s1, s12, s1
	s_cmp_lt_i32 s1, s0
	s_cbranch_scc1 .LBB0_850
	s_add_u32 s6, s48, 0xc100
	s_waitcnt vmcnt(0)
	v_lshlrev_b32_e32 v14, 4, v0
	v_mov_b32_e32 v15, 0
	s_addc_u32 s7, s49, 0
	v_lshl_add_u64 v[2:3], s[10:11], 0, v[14:15]
	s_mov_b64 s[10:11], 0x16600000
	s_add_i32 s1, 0, 0x27fd4
	v_cmp_eq_u32_e64 s[4:5], 0, v0
	s_mov_b32 s0, 4
	v_lshl_add_u64 v[16:17], v[2:3], 0, s[10:11]
	v_mov_b32_e32 v1, s1
	s_movk_i32 s16, 0x1ff
	s_branch .LBB0_844

.LBB0_848:
	s_or_b64 exec, exec, s[10:11]
	s_waitcnt lgkmcnt(0)
	s_barrier
	ds_read_b32 v2, v1
	s_mov_b64 s[10:11], -1
	s_waitcnt lgkmcnt(0)
	v_cmp_lt_u32_e32 vcc, s16, v2
	s_cbranch_vccnz .LBB0_843
	v_lshlrev_b32_e32 v14, 14, v2
	v_lshl_add_u64 v[18:19], v[14:15], 4, v[16:17]
	v_mov_b32_e32 v20, 0x22800000
	v_cmp_lt_u32_e32 vcc, 0xff, v2
	s_nop 1
	v_cndmask_b32_e32 v20, 0, v20, vcc
	v_add_co_u32_e32 v18, vcc, v18, v20
	s_nop 1
	v_addc_co_u32_e32 v19, vcc, 0, v19, vcc
	v_add_co_u32_e32 v2, vcc, 0x2000, v18
	s_add_i32 s0, s0, -1
	s_nop 0
	v_addc_co_u32_e32 v3, vcc, 0, v19, vcc
	global_load_dwordx4 v[20:23], v[18:19], off
	global_load_dwordx4 v[24:27], v[2:3], off
	v_add_co_u32_e32 v2, vcc, 0x4000, v18
	s_cmp_eq_u32 s0, 0
	s_nop 0
	v_addc_co_u32_e32 v3, vcc, 0, v19, vcc
	v_add_co_u32_e32 v4, vcc, 0x6000, v18
	s_cselect_b64 s[10:11], -1, 0
	s_nop 0
	v_addc_co_u32_e32 v5, vcc, 0, v19, vcc
	global_load_dwordx4 v[28:31], v[2:3], off
	global_load_dwordx4 v[32:35], v[4:5], off
	v_add_co_u32_e32 v2, vcc, 0x8000, v18
	s_waitcnt vmcnt(3)
	v_xor_b32_e32 v14, v21, v20
	v_addc_co_u32_e32 v3, vcc, 0, v19, vcc
	v_add_co_u32_e32 v4, vcc, 0xa000, v18
	v_xor_b32_e32 v14, v14, v23
	s_nop 0
	v_addc_co_u32_e32 v5, vcc, 0, v19, vcc
	global_load_dwordx4 v[36:39], v[2:3], off
	global_load_dwordx4 v[40:43], v[4:5], off
	v_add_co_u32_e32 v2, vcc, 0xc000, v18
	v_xor_b32_e32 v14, v14, v22
	s_nop 0
	v_addc_co_u32_e32 v3, vcc, 0, v19, vcc
	v_add_co_u32_e32 v4, vcc, 0xe000, v18
	s_waitcnt vmcnt(4)
	v_xor_b32_e32 v14, v25, v14
	v_addc_co_u32_e32 v5, vcc, 0, v19, vcc
	global_load_dwordx4 v[44:47], v[2:3], off
	global_load_dwordx4 v[48:51], v[4:5], off
	v_add_co_u32_e32 v2, vcc, 0x10000, v18
	v_xor_b32_e32 v14, v14, v24
	s_nop 0
	v_addc_co_u32_e32 v3, vcc, 0, v19, vcc
	v_add_co_u32_e32 v4, vcc, 0x12000, v18
	v_xor_b32_e32 v14, v14, v27
	s_nop 0
	v_addc_co_u32_e32 v5, vcc, 0, v19, vcc
	global_load_dwordx4 v[52:55], v[2:3], off
	global_load_dwordx4 v[56:59], v[4:5], off
	v_add_co_u32_e32 v2, vcc, 0x14000, v18
	v_xor_b32_e32 v14, v14, v26
	s_nop 0
	v_addc_co_u32_e32 v3, vcc, 0, v19, vcc
	global_load_dwordx4 v[60:63], v[2:3], off
	v_add_co_u32_e32 v2, vcc, 0x16000, v18
	s_waitcnt vmcnt(8)
	v_xor_b32_e32 v14, v29, v14
	v_addc_co_u32_e32 v3, vcc, 0, v19, vcc
	global_load_dwordx4 v[2:5], v[2:3], off
	v_add_co_u32_e32 v64, vcc, 0x18000, v18
	v_xor_b32_e32 v14, v14, v28
	s_nop 0
	v_addc_co_u32_e32 v65, vcc, 0, v19, vcc
	v_add_co_u32_e32 v66, vcc, 0x1a000, v18
	v_xor_b32_e32 v14, v14, v31
	s_nop 0
	v_addc_co_u32_e32 v67, vcc, 0, v19, vcc
	global_load_dwordx4 v[10:13], v[64:65], off
	global_load_dwordx4 v[6:9], v[66:67], off
	v_add_co_u32_e32 v28, vcc, 0x1c000, v18
	v_xor_b32_e32 v14, v14, v30
	s_nop 0
	v_addc_co_u32_e32 v29, vcc, 0, v19, vcc
	v_add_co_u32_e32 v30, vcc, 0x1e000, v18
	s_waitcnt vmcnt(10)
	v_xor_b32_e32 v14, v33, v14
	v_addc_co_u32_e32 v31, vcc, 0, v19, vcc
	global_load_dwordx4 v[20:23], v[28:29], off
	global_load_dwordx4 v[24:27], v[30:31], off
	v_xor_b32_e32 v14, v14, v32
	v_xor_b32_e32 v14, v14, v35
	v_xor_b32_e32 v14, v14, v34
	s_waitcnt vmcnt(11)
	v_xor_b32_e32 v14, v37, v14
	v_xor_b32_e32 v14, v14, v36
	v_add_co_u32_e32 v36, vcc, 0x20000, v18
	v_xor_b32_e32 v14, v14, v39
	s_nop 0
	v_addc_co_u32_e32 v37, vcc, 0, v19, vcc
	v_xor_b32_e32 v14, v14, v38
	v_add_co_u32_e32 v38, vcc, 0x22000, v18
	s_waitcnt vmcnt(10)
	v_xor_b32_e32 v14, v41, v14
	v_addc_co_u32_e32 v39, vcc, 0, v19, vcc
	global_load_dwordx4 v[28:31], v[36:37], off
	global_load_dwordx4 v[32:35], v[38:39], off
	v_xor_b32_e32 v14, v14, v40
	v_xor_b32_e32 v14, v14, v43
	v_xor_b32_e32 v14, v14, v42
	s_waitcnt vmcnt(11)
	v_xor_b32_e32 v14, v45, v14
	v_xor_b32_e32 v14, v14, v44
	v_add_co_u32_e32 v44, vcc, 0x24000, v18
	v_xor_b32_e32 v14, v14, v47
	s_nop 0
	v_addc_co_u32_e32 v45, vcc, 0, v19, vcc
	v_xor_b32_e32 v14, v14, v46
	v_add_co_u32_e32 v46, vcc, 0x26000, v18
	s_waitcnt vmcnt(10)
	v_xor_b32_e32 v14, v49, v14
	v_addc_co_u32_e32 v47, vcc, 0, v19, vcc
	global_load_dwordx4 v[36:39], v[44:45], off
	global_load_dwordx4 v[40:43], v[46:47], off
	v_xor_b32_e32 v14, v14, v48
	v_xor_b32_e32 v14, v14, v51
	v_xor_b32_e32 v14, v14, v50
	s_waitcnt vmcnt(11)
	v_xor_b32_e32 v14, v53, v14
	v_xor_b32_e32 v14, v14, v52
	v_add_co_u32_e32 v52, vcc, 0x28000, v18
	v_xor_b32_e32 v14, v14, v55
	s_nop 0
	v_addc_co_u32_e32 v53, vcc, 0, v19, vcc
	v_xor_b32_e32 v14, v14, v54
	v_add_co_u32_e32 v54, vcc, 0x2a000, v18
	s_waitcnt vmcnt(10)
	v_xor_b32_e32 v14, v57, v14
	v_addc_co_u32_e32 v55, vcc, 0, v19, vcc
	global_load_dwordx4 v[44:47], v[52:53], off
	global_load_dwordx4 v[48:51], v[54:55], off
	v_xor_b32_e32 v14, v14, v56
	v_xor_b32_e32 v14, v14, v59
	v_xor_b32_e32 v14, v14, v58
	s_waitcnt vmcnt(11)
	v_xor_b32_e32 v14, v61, v14
	v_xor_b32_e32 v14, v14, v60
	v_add_co_u32_e32 v60, vcc, 0x2c000, v18
	v_xor_b32_e32 v14, v14, v63
	s_nop 0
	v_addc_co_u32_e32 v61, vcc, 0, v19, vcc
	v_xor_b32_e32 v14, v14, v62
	v_add_co_u32_e32 v62, vcc, 0x2e000, v18
	s_waitcnt vmcnt(10)
	v_xor_b32_e32 v3, v3, v14
	v_addc_co_u32_e32 v63, vcc, 0, v19, vcc
	global_load_dwordx4 v[52:55], v[60:61], off
	global_load_dwordx4 v[56:59], v[62:63], off
	v_add_co_u32_e32 v68, vcc, 0x30000, v18
	v_xor_b32_e32 v2, v3, v2
	s_nop 0
	v_addc_co_u32_e32 v69, vcc, 0, v19, vcc
	v_add_co_u32_e32 v70, vcc, 0x32000, v18
	v_xor_b32_e32 v2, v2, v5
	s_nop 0
	v_addc_co_u32_e32 v71, vcc, 0, v19, vcc
	global_load_dwordx4 v[60:63], v[68:69], off
	global_load_dwordx4 v[64:67], v[70:71], off
	v_add_co_u32_e32 v76, vcc, 0x34000, v18
	v_xor_b32_e32 v2, v2, v4
	s_nop 0
	v_addc_co_u32_e32 v77, vcc, 0, v19, vcc
	v_add_co_u32_e32 v78, vcc, 0x36000, v18
	s_waitcnt vmcnt(13)
	v_xor_b32_e32 v2, v11, v2
	v_addc_co_u32_e32 v79, vcc, 0, v19, vcc
	global_load_dwordx4 v[68:71], v[76:77], off
	global_load_dwordx4 v[72:75], v[78:79], off
	v_add_co_u32_e32 v84, vcc, 0x38000, v18
	v_xor_b32_e32 v2, v2, v10
	s_nop 0
	v_addc_co_u32_e32 v85, vcc, 0, v19, vcc
	v_add_co_u32_e32 v86, vcc, 0x3a000, v18
	v_xor_b32_e32 v2, v2, v13
	s_nop 0
	v_addc_co_u32_e32 v87, vcc, 0, v19, vcc
	global_load_dwordx4 v[76:79], v[84:85], off
	global_load_dwordx4 v[80:83], v[86:87], off
	v_add_co_u32_e32 v84, vcc, 0x3c000, v18
	v_xor_b32_e32 v2, v2, v12
	s_nop 0
	v_addc_co_u32_e32 v85, vcc, 0, v19, vcc
	global_load_dwordx4 v[84:87], v[84:85], off
	v_add_co_u32_e32 v18, vcc, 0x3e000, v18
	s_waitcnt vmcnt(17)
	v_xor_b32_e32 v2, v7, v2
	v_addc_co_u32_e32 v19, vcc, 0, v19, vcc
	global_load_dwordx4 v[88:91], v[18:19], off
	v_xor_b32_e32 v2, v2, v6
	v_xor_b32_e32 v2, v2, v9
	v_xor_b32_e32 v2, v2, v8
	s_waitcnt vmcnt(17)
	v_xor_b32_e32 v2, v21, v2
	v_xor_b32_e32 v2, v2, v20
	v_xor_b32_e32 v2, v2, v23
	v_xor_b32_e32 v2, v2, v22
	s_waitcnt vmcnt(16)
	v_xor_b32_e32 v2, v25, v2
	v_xor_b32_e32 v2, v2, v24
	v_xor_b32_e32 v2, v2, v27
	v_xor_b32_e32 v2, v2, v26
	s_waitcnt vmcnt(15)
	v_xor_b32_e32 v2, v29, v2
	v_xor_b32_e32 v2, v2, v28
	v_xor_b32_e32 v2, v2, v31
	v_xor_b32_e32 v2, v2, v30
	s_waitcnt vmcnt(14)
	v_xor_b32_e32 v2, v33, v2
	v_xor_b32_e32 v2, v2, v32
	v_xor_b32_e32 v2, v2, v35
	v_xor_b32_e32 v2, v2, v34
	s_waitcnt vmcnt(13)
	v_xor_b32_e32 v2, v37, v2
	v_xor_b32_e32 v2, v2, v36
	v_xor_b32_e32 v2, v2, v39
	v_xor_b32_e32 v2, v2, v38
	s_waitcnt vmcnt(12)
	v_xor_b32_e32 v2, v41, v2
	v_xor_b32_e32 v2, v2, v40
	v_xor_b32_e32 v2, v2, v43
	v_xor_b32_e32 v2, v2, v42
	s_waitcnt vmcnt(11)
	v_xor_b32_e32 v2, v45, v2
	v_xor_b32_e32 v2, v2, v44
	v_xor_b32_e32 v2, v2, v47
	v_xor_b32_e32 v2, v2, v46
	s_waitcnt vmcnt(10)
	v_xor_b32_e32 v2, v49, v2
	v_xor_b32_e32 v2, v2, v48
	v_xor_b32_e32 v2, v2, v51
	v_xor_b32_e32 v2, v2, v50
	s_waitcnt vmcnt(9)
	v_xor_b32_e32 v2, v53, v2
	v_xor_b32_e32 v2, v2, v52
	v_xor_b32_e32 v2, v2, v55
	v_xor_b32_e32 v2, v2, v54
	s_waitcnt vmcnt(8)
	v_xor_b32_e32 v2, v57, v2
	v_xor_b32_e32 v2, v2, v56
	v_xor_b32_e32 v2, v2, v59
	v_xor_b32_e32 v2, v2, v58
	s_waitcnt vmcnt(7)
	v_xor_b32_e32 v2, v61, v2
	v_xor_b32_e32 v2, v2, v60
	v_xor_b32_e32 v2, v2, v63
	v_xor_b32_e32 v2, v2, v62
	s_waitcnt vmcnt(6)
	v_xor_b32_e32 v2, v65, v2
	v_xor_b32_e32 v2, v2, v64
	v_xor_b32_e32 v2, v2, v67
	v_xor_b32_e32 v2, v2, v66
	s_waitcnt vmcnt(5)
	v_xor_b32_e32 v2, v69, v2
	v_xor_b32_e32 v2, v2, v68
	v_xor_b32_e32 v2, v2, v71
	v_xor_b32_e32 v2, v2, v70
	s_waitcnt vmcnt(4)
	v_xor_b32_e32 v2, v73, v2
	v_xor_b32_e32 v2, v2, v72
	v_xor_b32_e32 v2, v2, v75
	v_xor_b32_e32 v2, v2, v74
	s_waitcnt vmcnt(3)
	v_xor_b32_e32 v2, v77, v2
	v_xor_b32_e32 v2, v2, v76
	v_xor_b32_e32 v2, v2, v79
	v_xor_b32_e32 v2, v2, v78
	s_waitcnt vmcnt(2)
	v_xor_b32_e32 v2, v81, v2
	v_xor_b32_e32 v2, v2, v80
	v_xor_b32_e32 v2, v2, v83
	v_xor_b32_e32 v2, v2, v82
	s_waitcnt vmcnt(1)
	v_xor_b32_e32 v2, v85, v2
	v_xor_b32_e32 v2, v2, v84
	v_xor_b32_e32 v2, v2, v87
	v_xor_b32_e32 v2, v2, v86
	s_waitcnt vmcnt(0)
	v_xor_b32_e32 v2, v89, v2
	v_xor_b32_e32 v2, v2, v88
	v_xor_b32_e32 v2, v2, v91
	v_xor_b32_e32 v2, v2, v90
	s_branch .LBB0_843
